# batch barrier-census loads; batch LDS reads in x1 un-sum; batch kmean row-group loads (counted vmcnt)
# baseline (speedup 1.0000x reference)
; __device__ __forceinline__ void moba_kmean_wave(int item, int b0, const h16* __restrict__ proj, float* __restrict__ kmean) {
;     ...
;     const h16* kp = proj + ((size_t)bl * SEQ + blk * 256 + r8) * PP + PC_BK + h * 64 + c8 * 8;
;     float acc[8];
; #pragma unroll
;     for (int e = 0; e < 8; ++e) acc[e] = 0.f;
; #pragma unroll 8
;     for (int j = 0; j < 32; ++j) { const h16x8 v = *(const h16x8*)(kp + (size_t)(8 * j) * PP);
; #pragma unroll
;         for (int e = 0; e < 8; ++e) acc[e] += (float)v[e]; }
.LBB0_938:
	v_lshl_add_u64 v[14:15], v[0:1], 0, s[0:1]
	v_add_co_u32_e32 v52, vcc, 0xc401000, v14
	s_nop 1
	v_addc_co_u32_e32 v53, vcc, 0, v15, vcc
	global_load_dwordx4 v[20:23], v[52:53], off offset:1024
	v_add_co_u32_e32 v52, vcc, 0xc41d000, v14
	s_nop 1
	v_addc_co_u32_e32 v53, vcc, 0, v15, vcc
	global_load_dwordx4 v[24:27], v[52:53], off offset:1024
	v_add_co_u32_e32 v52, vcc, 0xc439000, v14
	s_nop 1
	v_addc_co_u32_e32 v53, vcc, 0, v15, vcc
	global_load_dwordx4 v[28:31], v[52:53], off offset:1024
	v_add_co_u32_e32 v52, vcc, 0xc455000, v14
	s_nop 1
	v_addc_co_u32_e32 v53, vcc, 0, v15, vcc
	global_load_dwordx4 v[32:35], v[52:53], off offset:1024
	v_add_co_u32_e32 v52, vcc, 0xc471000, v14
	s_nop 1
	v_addc_co_u32_e32 v53, vcc, 0, v15, vcc
	global_load_dwordx4 v[36:39], v[52:53], off offset:1024
	v_add_co_u32_e32 v52, vcc, 0xc48d000, v14
	s_nop 1
	v_addc_co_u32_e32 v53, vcc, 0, v15, vcc
	global_load_dwordx4 v[40:43], v[52:53], off offset:1024
	v_add_co_u32_e32 v52, vcc, 0xc4a9000, v14
	s_nop 1
	v_addc_co_u32_e32 v53, vcc, 0, v15, vcc
	global_load_dwordx4 v[44:47], v[52:53], off offset:1024
	v_add_co_u32_e32 v52, vcc, 0xc4c5000, v14
	s_nop 1
	v_addc_co_u32_e32 v53, vcc, 0, v15, vcc
	global_load_dwordx4 v[48:51], v[52:53], off offset:1024
	s_add_u32 s0, s0, 0xe0000
	s_addc_u32 s1, s1, 0
	s_cmp_lg_u32 s0, 0x380000
	s_waitcnt vmcnt(7)
	v_cvt_f32_f16_e32 v18, v20
	v_cvt_f32_f16_sdwa v19, v20 dst_sel:DWORD dst_unused:UNUSED_PAD src0_sel:WORD_1
	v_pk_add_f32 v[8:9], v[8:9], v[18:19]
	v_cvt_f32_f16_e32 v18, v21
	v_cvt_f32_f16_sdwa v19, v21 dst_sel:DWORD dst_unused:UNUSED_PAD src0_sel:WORD_1
	v_pk_add_f32 v[6:7], v[6:7], v[18:19]
	v_cvt_f32_f16_e32 v18, v22
	v_cvt_f32_f16_sdwa v19, v22 dst_sel:DWORD dst_unused:UNUSED_PAD src0_sel:WORD_1
	v_pk_add_f32 v[4:5], v[4:5], v[18:19]
	v_cvt_f32_f16_e32 v18, v23
	v_cvt_f32_f16_sdwa v19, v23 dst_sel:DWORD dst_unused:UNUSED_PAD src0_sel:WORD_1
	v_pk_add_f32 v[2:3], v[2:3], v[18:19]
	s_waitcnt vmcnt(6)
	v_cvt_f32_f16_e32 v18, v24
	v_cvt_f32_f16_sdwa v19, v24 dst_sel:DWORD dst_unused:UNUSED_PAD src0_sel:WORD_1
	v_pk_add_f32 v[8:9], v[8:9], v[18:19]
	v_cvt_f32_f16_e32 v18, v25
	v_cvt_f32_f16_sdwa v19, v25 dst_sel:DWORD dst_unused:UNUSED_PAD src0_sel:WORD_1
	v_pk_add_f32 v[6:7], v[6:7], v[18:19]
	v_cvt_f32_f16_e32 v18, v26
	v_cvt_f32_f16_sdwa v19, v26 dst_sel:DWORD dst_unused:UNUSED_PAD src0_sel:WORD_1
	v_pk_add_f32 v[4:5], v[4:5], v[18:19]
	v_cvt_f32_f16_e32 v18, v27
	v_cvt_f32_f16_sdwa v19, v27 dst_sel:DWORD dst_unused:UNUSED_PAD src0_sel:WORD_1
	v_pk_add_f32 v[2:3], v[2:3], v[18:19]
	s_waitcnt vmcnt(5)
	v_cvt_f32_f16_e32 v18, v28
	v_cvt_f32_f16_sdwa v19, v28 dst_sel:DWORD dst_unused:UNUSED_PAD src0_sel:WORD_1
	v_pk_add_f32 v[8:9], v[8:9], v[18:19]
	v_cvt_f32_f16_e32 v18, v29
	v_cvt_f32_f16_sdwa v19, v29 dst_sel:DWORD dst_unused:UNUSED_PAD src0_sel:WORD_1
	v_pk_add_f32 v[6:7], v[6:7], v[18:19]
	v_cvt_f32_f16_e32 v18, v30
	v_cvt_f32_f16_sdwa v19, v30 dst_sel:DWORD dst_unused:UNUSED_PAD src0_sel:WORD_1
	v_pk_add_f32 v[4:5], v[4:5], v[18:19]
	v_cvt_f32_f16_e32 v18, v31
	v_cvt_f32_f16_sdwa v19, v31 dst_sel:DWORD dst_unused:UNUSED_PAD src0_sel:WORD_1
	v_pk_add_f32 v[2:3], v[2:3], v[18:19]
	s_waitcnt vmcnt(4)
	v_cvt_f32_f16_e32 v18, v32
	v_cvt_f32_f16_sdwa v19, v32 dst_sel:DWORD dst_unused:UNUSED_PAD src0_sel:WORD_1
	v_pk_add_f32 v[8:9], v[8:9], v[18:19]
	v_cvt_f32_f16_e32 v18, v33
	v_cvt_f32_f16_sdwa v19, v33 dst_sel:DWORD dst_unused:UNUSED_PAD src0_sel:WORD_1
	v_pk_add_f32 v[6:7], v[6:7], v[18:19]
	v_cvt_f32_f16_e32 v18, v34
	v_cvt_f32_f16_sdwa v19, v34 dst_sel:DWORD dst_unused:UNUSED_PAD src0_sel:WORD_1
	v_pk_add_f32 v[4:5], v[4:5], v[18:19]
	v_cvt_f32_f16_e32 v18, v35
	v_cvt_f32_f16_sdwa v19, v35 dst_sel:DWORD dst_unused:UNUSED_PAD src0_sel:WORD_1
	v_pk_add_f32 v[2:3], v[2:3], v[18:19]
	s_waitcnt vmcnt(3)
	v_cvt_f32_f16_e32 v18, v36
	v_cvt_f32_f16_sdwa v19, v36 dst_sel:DWORD dst_unused:UNUSED_PAD src0_sel:WORD_1
	v_pk_add_f32 v[8:9], v[8:9], v[18:19]
	v_cvt_f32_f16_e32 v18, v37
	v_cvt_f32_f16_sdwa v19, v37 dst_sel:DWORD dst_unused:UNUSED_PAD src0_sel:WORD_1
	v_pk_add_f32 v[6:7], v[6:7], v[18:19]
	v_cvt_f32_f16_e32 v18, v38
	v_cvt_f32_f16_sdwa v19, v38 dst_sel:DWORD dst_unused:UNUSED_PAD src0_sel:WORD_1
	v_pk_add_f32 v[4:5], v[4:5], v[18:19]
	v_cvt_f32_f16_e32 v18, v39
	v_cvt_f32_f16_sdwa v19, v39 dst_sel:DWORD dst_unused:UNUSED_PAD src0_sel:WORD_1
	v_pk_add_f32 v[2:3], v[2:3], v[18:19]
	s_waitcnt vmcnt(2)
	v_cvt_f32_f16_e32 v18, v40
	v_cvt_f32_f16_sdwa v19, v40 dst_sel:DWORD dst_unused:UNUSED_PAD src0_sel:WORD_1
	v_pk_add_f32 v[8:9], v[8:9], v[18:19]
	v_cvt_f32_f16_e32 v18, v41
	v_cvt_f32_f16_sdwa v19, v41 dst_sel:DWORD dst_unused:UNUSED_PAD src0_sel:WORD_1
	v_pk_add_f32 v[6:7], v[6:7], v[18:19]
	v_cvt_f32_f16_e32 v18, v42
	v_cvt_f32_f16_sdwa v19, v42 dst_sel:DWORD dst_unused:UNUSED_PAD src0_sel:WORD_1
	v_pk_add_f32 v[4:5], v[4:5], v[18:19]
	v_cvt_f32_f16_e32 v18, v43
	v_cvt_f32_f16_sdwa v19, v43 dst_sel:DWORD dst_unused:UNUSED_PAD src0_sel:WORD_1
	v_pk_add_f32 v[2:3], v[2:3], v[18:19]
	s_waitcnt vmcnt(1)
	v_cvt_f32_f16_e32 v18, v44
	v_cvt_f32_f16_sdwa v19, v44 dst_sel:DWORD dst_unused:UNUSED_PAD src0_sel:WORD_1
	v_pk_add_f32 v[8:9], v[8:9], v[18:19]
	v_cvt_f32_f16_e32 v18, v45
	v_cvt_f32_f16_sdwa v19, v45 dst_sel:DWORD dst_unused:UNUSED_PAD src0_sel:WORD_1
	v_pk_add_f32 v[6:7], v[6:7], v[18:19]
	v_cvt_f32_f16_e32 v18, v46
	v_cvt_f32_f16_sdwa v19, v46 dst_sel:DWORD dst_unused:UNUSED_PAD src0_sel:WORD_1
	v_pk_add_f32 v[4:5], v[4:5], v[18:19]
	v_cvt_f32_f16_e32 v18, v47
	v_cvt_f32_f16_sdwa v19, v47 dst_sel:DWORD dst_unused:UNUSED_PAD src0_sel:WORD_1
	v_pk_add_f32 v[2:3], v[2:3], v[18:19]
	s_waitcnt vmcnt(0)
	v_cvt_f32_f16_e32 v18, v48
	v_cvt_f32_f16_sdwa v19, v48 dst_sel:DWORD dst_unused:UNUSED_PAD src0_sel:WORD_1
	v_pk_add_f32 v[8:9], v[8:9], v[18:19]
	v_cvt_f32_f16_e32 v18, v49
	v_cvt_f32_f16_sdwa v19, v49 dst_sel:DWORD dst_unused:UNUSED_PAD src0_sel:WORD_1
	v_pk_add_f32 v[6:7], v[6:7], v[18:19]
	v_cvt_f32_f16_e32 v18, v50
	v_cvt_f32_f16_sdwa v19, v50 dst_sel:DWORD dst_unused:UNUSED_PAD src0_sel:WORD_1
	v_pk_add_f32 v[4:5], v[4:5], v[18:19]
	v_cvt_f32_f16_e32 v18, v51
	v_cvt_f32_f16_sdwa v19, v51 dst_sel:DWORD dst_unused:UNUSED_PAD src0_sel:WORD_1
	v_pk_add_f32 v[2:3], v[2:3], v[18:19]
	s_cbranch_scc1 .LBB0_938
; template <int M> __device__ __forceinline__ float swz_xor(float v) { return __int_as_float(__builtin_amdgcn_ds_swizzle(__float_as_int(v), (M << 10) | 0x1f)); }
; __device__ __forceinline__ float half_sum(float v) { auto rr = __builtin_amdgcn_permlane32_swap(__float_as_uint(v), __float_as_uint(v), false, false); return __uint_as_float(rr[0]) + __uint_as_float(rr[1]); }
; __device__ __forceinline__ void moba_kmean_wave(int item, int b0, const h16* __restrict__ proj, float* __restrict__ kmean) {
;     ...
;     for (int e = 0; e < 8; ++e) { acc[e] += swz_xor<8>(acc[e]); acc[e] += swz_xor<16>(acc[e]); acc[e] = half_sum(acc[e]); }
;     if (r8 == 0) { float* op = kmean + (((size_t)(b0 + bl) * 8 + h) * 8 + blk) * 64 + c8 * 8;
;         *(f32x4*)op = (f32x4){acc[0], acc[1], acc[2], acc[3]} * (1.f / 256.f); *(f32x4*)(op + 4) = (f32x4){acc[4], acc[5], acc[6], acc[7]} * (1.f / 256.f); }
	ds_swizzle_b32 v0, v8 offset:swizzle(SWAP,8)
	ds_swizzle_b32 v1, v9 offset:swizzle(SWAP,8)
	ds_swizzle_b32 v10, v6 offset:swizzle(SWAP,8)
	ds_swizzle_b32 v11, v7 offset:swizzle(SWAP,8)
	ds_swizzle_b32 v12, v4 offset:swizzle(SWAP,8)
	ds_swizzle_b32 v13, v5 offset:swizzle(SWAP,8)
	ds_swizzle_b32 v14, v2 offset:swizzle(SWAP,8)
	ds_swizzle_b32 v15, v3 offset:swizzle(SWAP,8)
	s_waitcnt lgkmcnt(0)
	v_add_f32_e32 v0, v8, v0
	v_add_f32_e32 v1, v9, v1
	v_add_f32_e32 v6, v6, v10
	v_add_f32_e32 v7, v7, v11
	v_add_f32_e32 v4, v4, v12
	v_add_f32_e32 v5, v5, v13
	v_add_f32_e32 v2, v2, v14
	v_add_f32_e32 v3, v3, v15
	ds_swizzle_b32 v8, v0 offset:swizzle(SWAP,16)
	ds_swizzle_b32 v9, v1 offset:swizzle(SWAP,16)
	ds_swizzle_b32 v10, v6 offset:swizzle(SWAP,16)
	ds_swizzle_b32 v11, v7 offset:swizzle(SWAP,16)
	ds_swizzle_b32 v12, v4 offset:swizzle(SWAP,16)
	ds_swizzle_b32 v13, v5 offset:swizzle(SWAP,16)
	ds_swizzle_b32 v14, v2 offset:swizzle(SWAP,16)
	ds_swizzle_b32 v15, v3 offset:swizzle(SWAP,16)
	s_waitcnt lgkmcnt(7)
	v_add_f32_e32 v0, v0, v8
	s_waitcnt lgkmcnt(6)
	v_add_f32_e32 v1, v1, v9
	s_waitcnt lgkmcnt(5)
	v_add_f32_e32 v6, v6, v10
	s_waitcnt lgkmcnt(4)
	v_add_f32_e32 v7, v7, v11
	s_waitcnt lgkmcnt(3)
	v_add_f32_e32 v4, v4, v12
	s_waitcnt lgkmcnt(2)
	v_add_f32_e32 v5, v5, v13
	s_waitcnt lgkmcnt(1)
	v_add_f32_e32 v2, v2, v14
	s_waitcnt lgkmcnt(0)
	v_add_f32_e32 v3, v3, v15
	v_mov_b32_e32 v8, v0
	v_mov_b32_e32 v9, v1
	v_mov_b32_e32 v10, v6
	v_mov_b32_e32 v11, v7
	v_mov_b32_e32 v12, v4
	v_mov_b32_e32 v13, v5
	v_mov_b32_e32 v14, v2
	v_mov_b32_e32 v15, v3
	v_permlane32_swap_b32_e32 v0, v8
	v_permlane32_swap_b32_e32 v1, v9
	v_permlane32_swap_b32_e32 v6, v10
	v_permlane32_swap_b32_e32 v7, v11
	v_permlane32_swap_b32_e32 v4, v12
	v_permlane32_swap_b32_e32 v5, v13
	v_permlane32_swap_b32_e32 v2, v14
	v_permlane32_swap_b32_e32 v3, v15
	v_cmp_gt_u32_e32 vcc, 8, v16
	s_and_saveexec_b64 s[0:1], vcc
	s_cbranch_execz .LBB0_941
	s_add_i32 s6, s6, s4
	s_lshl_b32 s6, s6, 6
	s_lshl_b32 s10, s3, 3
	s_or_b32 s6, s6, s10
	s_or_b32 s5, s6, s5
	s_lshl_b32 s28, s5, 6
	s_lshl_b64 s[10:11], s[28:29], 2
	v_readlane_b32 s5, v254, 10
	v_pk_add_f32 v[0:1], v[0:1], v[8:9]
	v_pk_add_f32 v[6:7], v[6:7], v[10:11]
	v_pk_add_f32 v[8:9], v[2:3], v[14:15]
	s_add_u32 s10, s5, s10
	v_readlane_b32 s5, v254, 11
	v_lshlrev_b32_e32 v2, 5, v16
	s_mov_b32 s6, 0x3b800000
	v_pk_add_f32 v[4:5], v[4:5], v[12:13]
	s_addc_u32 s11, s5, s11
	v_and_b32_e32 v10, 0xe0, v2
	v_pk_mul_f32 v[2:3], v[6:7], s[6:7] op_sel_hi:[1,0]
	v_pk_mul_f32 v[0:1], v[0:1], s[6:7] op_sel_hi:[1,0]
	global_store_dwordx4 v10, v[0:3], s[10:11]
	s_nop 1
	v_pk_mul_f32 v[2:3], v[8:9], s[6:7] op_sel_hi:[1,0]
	v_pk_mul_f32 v[0:1], v[4:5], s[6:7] op_sel_hi:[1,0]
	global_store_dwordx4 v10, v[0:3], s[10:11] offset:16
